# P0 adaLN: the 18 silu(c) inputs of a thread requested together before the arithmetic (was 18 dependent load-compute round trips)
# speedup vs baseline: 1.0033x; 1.0033x over previous
.LBB0_17:
	s_cmpk_gt_i32 s93, 0xbf
	s_cbranch_scc1 .LBB0_31
	s_and_saveexec_b64 s[8:9], s[0:1]
	s_cbranch_execz .LBB0_25
	ds_read_b32 v4, v5 offset:520
	ds_read_b32 v68, v5 offset:524
	ds_read_b32 v69, v5 offset:536
	ds_read_b32 v72, v5 offset:540
	v_mov_b64_e32 v[66:67], v[58:59]
	s_waitcnt lgkmcnt(0)
	v_readfirstlane_b32 s22, v4
	v_readfirstlane_b32 s23, v68
	v_readfirstlane_b32 s20, v69
	v_readfirstlane_b32 s21, v72
	s_nop 1
	v_lshl_add_u64 v[68:69], s[22:23], 0, v[66:67]
	global_load_dword v104, v[68:69], off
	v_lshl_add_u64 v[66:67], v[66:67], 0, s[64:65]
	v_lshl_add_u64 v[68:69], s[22:23], 0, v[66:67]
	global_load_dword v105, v[68:69], off
	v_lshl_add_u64 v[66:67], v[66:67], 0, s[64:65]
	v_lshl_add_u64 v[68:69], s[22:23], 0, v[66:67]
	global_load_dword v106, v[68:69], off
	v_lshl_add_u64 v[66:67], v[66:67], 0, s[64:65]
	v_lshl_add_u64 v[68:69], s[22:23], 0, v[66:67]
	global_load_dword v107, v[68:69], off
	v_lshl_add_u64 v[66:67], v[66:67], 0, s[64:65]
	v_lshl_add_u64 v[68:69], s[22:23], 0, v[66:67]
	global_load_dword v108, v[68:69], off
	v_lshl_add_u64 v[66:67], v[66:67], 0, s[64:65]
	v_lshl_add_u64 v[68:69], s[22:23], 0, v[66:67]
	global_load_dword v109, v[68:69], off
	v_lshl_add_u64 v[66:67], v[66:67], 0, s[64:65]
	v_lshl_add_u64 v[68:69], s[22:23], 0, v[66:67]
	global_load_dword v110, v[68:69], off
	v_lshl_add_u64 v[66:67], v[66:67], 0, s[64:65]
	v_lshl_add_u64 v[68:69], s[22:23], 0, v[66:67]
	global_load_dword v111, v[68:69], off
	v_lshl_add_u64 v[66:67], v[66:67], 0, s[64:65]
	v_lshl_add_u64 v[68:69], s[22:23], 0, v[66:67]
	global_load_dword v112, v[68:69], off
	v_lshl_add_u64 v[66:67], v[66:67], 0, s[64:65]
	v_lshl_add_u64 v[68:69], s[22:23], 0, v[66:67]
	global_load_dword v113, v[68:69], off
	v_lshl_add_u64 v[66:67], v[66:67], 0, s[64:65]
	v_lshl_add_u64 v[68:69], s[22:23], 0, v[66:67]
	global_load_dword v114, v[68:69], off
	v_lshl_add_u64 v[66:67], v[66:67], 0, s[64:65]
	v_lshl_add_u64 v[68:69], s[22:23], 0, v[66:67]
	global_load_dword v115, v[68:69], off
	v_lshl_add_u64 v[66:67], v[66:67], 0, s[64:65]
	v_lshl_add_u64 v[68:69], s[22:23], 0, v[66:67]
	global_load_dword v116, v[68:69], off
	v_lshl_add_u64 v[66:67], v[66:67], 0, s[64:65]
	v_lshl_add_u64 v[68:69], s[22:23], 0, v[66:67]
	global_load_dword v117, v[68:69], off
	v_lshl_add_u64 v[66:67], v[66:67], 0, s[64:65]
	v_lshl_add_u64 v[68:69], s[22:23], 0, v[66:67]
	global_load_dword v118, v[68:69], off
	v_lshl_add_u64 v[66:67], v[66:67], 0, s[64:65]
	v_lshl_add_u64 v[68:69], s[22:23], 0, v[66:67]
	global_load_dword v119, v[68:69], off
	v_lshl_add_u64 v[66:67], v[66:67], 0, s[64:65]
	v_and_b32_e32 v69, 0x3ff, v0
	v_lshlrev_b32_e32 v4, 2, v69
	s_nop 0
	v_lshl_add_u64 v[68:69], s[20:21], 0, v[4:5]
	global_load_dword v120, v[68:69], off
	v_add_u32_e32 v69, 0x200, v0
	v_and_b32_e32 v69, 0x3ff, v69
	v_lshlrev_b32_e32 v4, 2, v69
	s_nop 0
	v_lshl_add_u64 v[68:69], s[20:21], 0, v[4:5]
	global_load_dword v121, v[68:69], off
	s_mov_b32 s6, 0xbfb8aa3b
	s_mov_b32 s7, 0x42ce8ed0
	s_mov_b32 s20, 0xc2b17218
	s_waitcnt vmcnt(17)
	v_mul_f32_e32 v68, 0xbfb8aa3b, v104
	v_rndne_f32_e32 v69, v68
	v_fma_f32 v72, v104, s6, -v68
	v_sub_f32_e32 v68, v68, v69
	v_fmac_f32_e32 v72, 0xb2a5705f, v104
	v_add_f32_e32 v68, v68, v72
	v_cvt_i32_f32_e32 v69, v69
	v_exp_f32_e32 v68, v68
	v_cmp_nlt_f32_e64 s[22:23], s7, v104
	s_nop 1
	v_ldexp_f32 v68, v68, v69
	v_cndmask_b32_e64 v68, 0, v68, s[22:23]
	v_cmp_ngt_f32_e64 s[22:23], s20, v104
	s_nop 1
	v_cndmask_b32_e64 v68, v97, v68, s[22:23]
	v_add_f32_e32 v68, 1.0, v68
	v_div_scale_f32 v69, s[22:23], v68, v68, v104
	v_rcp_f32_e32 v71, v69
	v_div_scale_f32 v73, vcc, v104, v68, v104
	v_fma_f32 v74, -v69, v71, 1.0
	v_fmac_f32_e32 v71, v74, v71
	v_mul_f32_e32 v74, v73, v71
	v_fma_f32 v75, -v69, v74, v73
	v_fmac_f32_e32 v74, v75, v71
	v_fma_f32 v69, -v69, v74, v73
	v_div_fmas_f32 v69, v69, v71, v74
	v_div_fixup_f32 v104, v69, v68, v104
	ds_write_b32 v33, v104 offset:0
	s_waitcnt vmcnt(16)
	v_mul_f32_e32 v68, 0xbfb8aa3b, v105
	v_rndne_f32_e32 v69, v68
	v_fma_f32 v72, v105, s6, -v68
	v_sub_f32_e32 v68, v68, v69
	v_fmac_f32_e32 v72, 0xb2a5705f, v105
	v_add_f32_e32 v68, v68, v72
	v_cvt_i32_f32_e32 v69, v69
	v_exp_f32_e32 v68, v68
	v_cmp_nlt_f32_e64 s[22:23], s7, v105
	s_nop 1
	v_ldexp_f32 v68, v68, v69
	v_cndmask_b32_e64 v68, 0, v68, s[22:23]
	v_cmp_ngt_f32_e64 s[22:23], s20, v105
	s_nop 1
	v_cndmask_b32_e64 v68, v97, v68, s[22:23]
	v_add_f32_e32 v68, 1.0, v68
	v_div_scale_f32 v69, s[22:23], v68, v68, v105
	v_rcp_f32_e32 v71, v69
	v_div_scale_f32 v73, vcc, v105, v68, v105
	v_fma_f32 v74, -v69, v71, 1.0
	v_fmac_f32_e32 v71, v74, v71
	v_mul_f32_e32 v74, v73, v71
	v_fma_f32 v75, -v69, v74, v73
	v_fmac_f32_e32 v74, v75, v71
	v_fma_f32 v69, -v69, v74, v73
	v_div_fmas_f32 v69, v69, v71, v74
	v_div_fixup_f32 v105, v69, v68, v105
	ds_write_b32 v33, v105 offset:2048
	s_waitcnt vmcnt(15)
	v_mul_f32_e32 v68, 0xbfb8aa3b, v106
	v_rndne_f32_e32 v69, v68
	v_fma_f32 v72, v106, s6, -v68
	v_sub_f32_e32 v68, v68, v69
	v_fmac_f32_e32 v72, 0xb2a5705f, v106
	v_add_f32_e32 v68, v68, v72
	v_cvt_i32_f32_e32 v69, v69
	v_exp_f32_e32 v68, v68
	v_cmp_nlt_f32_e64 s[22:23], s7, v106
	s_nop 1
	v_ldexp_f32 v68, v68, v69
	v_cndmask_b32_e64 v68, 0, v68, s[22:23]
	v_cmp_ngt_f32_e64 s[22:23], s20, v106
	s_nop 1
	v_cndmask_b32_e64 v68, v97, v68, s[22:23]
	v_add_f32_e32 v68, 1.0, v68
	v_div_scale_f32 v69, s[22:23], v68, v68, v106
	v_rcp_f32_e32 v71, v69
	v_div_scale_f32 v73, vcc, v106, v68, v106
	v_fma_f32 v74, -v69, v71, 1.0
	v_fmac_f32_e32 v71, v74, v71
	v_mul_f32_e32 v74, v73, v71
	v_fma_f32 v75, -v69, v74, v73
	v_fmac_f32_e32 v74, v75, v71
	v_fma_f32 v69, -v69, v74, v73
	v_div_fmas_f32 v69, v69, v71, v74
	v_div_fixup_f32 v106, v69, v68, v106
	ds_write_b32 v33, v106 offset:4096
	s_waitcnt vmcnt(14)
	v_mul_f32_e32 v68, 0xbfb8aa3b, v107
	v_rndne_f32_e32 v69, v68
	v_fma_f32 v72, v107, s6, -v68
	v_sub_f32_e32 v68, v68, v69
	v_fmac_f32_e32 v72, 0xb2a5705f, v107
	v_add_f32_e32 v68, v68, v72
	v_cvt_i32_f32_e32 v69, v69
	v_exp_f32_e32 v68, v68
	v_cmp_nlt_f32_e64 s[22:23], s7, v107
	s_nop 1
	v_ldexp_f32 v68, v68, v69
	v_cndmask_b32_e64 v68, 0, v68, s[22:23]
	v_cmp_ngt_f32_e64 s[22:23], s20, v107
	s_nop 1
	v_cndmask_b32_e64 v68, v97, v68, s[22:23]
	v_add_f32_e32 v68, 1.0, v68
	v_div_scale_f32 v69, s[22:23], v68, v68, v107
	v_rcp_f32_e32 v71, v69
	v_div_scale_f32 v73, vcc, v107, v68, v107
	v_fma_f32 v74, -v69, v71, 1.0
	v_fmac_f32_e32 v71, v74, v71
	v_mul_f32_e32 v74, v73, v71
	v_fma_f32 v75, -v69, v74, v73
	v_fmac_f32_e32 v74, v75, v71
	v_fma_f32 v69, -v69, v74, v73
	v_div_fmas_f32 v69, v69, v71, v74
	v_div_fixup_f32 v107, v69, v68, v107
	ds_write_b32 v33, v107 offset:6144
	s_waitcnt vmcnt(13)
	v_mul_f32_e32 v68, 0xbfb8aa3b, v108
	v_rndne_f32_e32 v69, v68
	v_fma_f32 v72, v108, s6, -v68
	v_sub_f32_e32 v68, v68, v69
	v_fmac_f32_e32 v72, 0xb2a5705f, v108
	v_add_f32_e32 v68, v68, v72
	v_cvt_i32_f32_e32 v69, v69
	v_exp_f32_e32 v68, v68
	v_cmp_nlt_f32_e64 s[22:23], s7, v108
	s_nop 1
	v_ldexp_f32 v68, v68, v69
	v_cndmask_b32_e64 v68, 0, v68, s[22:23]
	v_cmp_ngt_f32_e64 s[22:23], s20, v108
	s_nop 1
	v_cndmask_b32_e64 v68, v97, v68, s[22:23]
	v_add_f32_e32 v68, 1.0, v68
	v_div_scale_f32 v69, s[22:23], v68, v68, v108
	v_rcp_f32_e32 v71, v69
	v_div_scale_f32 v73, vcc, v108, v68, v108
	v_fma_f32 v74, -v69, v71, 1.0
	v_fmac_f32_e32 v71, v74, v71
	v_mul_f32_e32 v74, v73, v71
	v_fma_f32 v75, -v69, v74, v73
	v_fmac_f32_e32 v74, v75, v71
	v_fma_f32 v69, -v69, v74, v73
	v_div_fmas_f32 v69, v69, v71, v74
	v_div_fixup_f32 v108, v69, v68, v108
	ds_write_b32 v33, v108 offset:8192
	s_waitcnt vmcnt(12)
	v_mul_f32_e32 v68, 0xbfb8aa3b, v109
	v_rndne_f32_e32 v69, v68
	v_fma_f32 v72, v109, s6, -v68
	v_sub_f32_e32 v68, v68, v69
	v_fmac_f32_e32 v72, 0xb2a5705f, v109
	v_add_f32_e32 v68, v68, v72
	v_cvt_i32_f32_e32 v69, v69
	v_exp_f32_e32 v68, v68
	v_cmp_nlt_f32_e64 s[22:23], s7, v109
	s_nop 1
	v_ldexp_f32 v68, v68, v69
	v_cndmask_b32_e64 v68, 0, v68, s[22:23]
	v_cmp_ngt_f32_e64 s[22:23], s20, v109
	s_nop 1
	v_cndmask_b32_e64 v68, v97, v68, s[22:23]
	v_add_f32_e32 v68, 1.0, v68
	v_div_scale_f32 v69, s[22:23], v68, v68, v109
	v_rcp_f32_e32 v71, v69
	v_div_scale_f32 v73, vcc, v109, v68, v109
	v_fma_f32 v74, -v69, v71, 1.0
	v_fmac_f32_e32 v71, v74, v71
	v_mul_f32_e32 v74, v73, v71
	v_fma_f32 v75, -v69, v74, v73
	v_fmac_f32_e32 v74, v75, v71
	v_fma_f32 v69, -v69, v74, v73
	v_div_fmas_f32 v69, v69, v71, v74
	v_div_fixup_f32 v109, v69, v68, v109
	ds_write_b32 v33, v109 offset:10240
	s_waitcnt vmcnt(11)
	v_mul_f32_e32 v68, 0xbfb8aa3b, v110
	v_rndne_f32_e32 v69, v68
	v_fma_f32 v72, v110, s6, -v68
	v_sub_f32_e32 v68, v68, v69
	v_fmac_f32_e32 v72, 0xb2a5705f, v110
	v_add_f32_e32 v68, v68, v72
	v_cvt_i32_f32_e32 v69, v69
	v_exp_f32_e32 v68, v68
	v_cmp_nlt_f32_e64 s[22:23], s7, v110
	s_nop 1
	v_ldexp_f32 v68, v68, v69
	v_cndmask_b32_e64 v68, 0, v68, s[22:23]
	v_cmp_ngt_f32_e64 s[22:23], s20, v110
	s_nop 1
	v_cndmask_b32_e64 v68, v97, v68, s[22:23]
	v_add_f32_e32 v68, 1.0, v68
	v_div_scale_f32 v69, s[22:23], v68, v68, v110
	v_rcp_f32_e32 v71, v69
	v_div_scale_f32 v73, vcc, v110, v68, v110
	v_fma_f32 v74, -v69, v71, 1.0
	v_fmac_f32_e32 v71, v74, v71
	v_mul_f32_e32 v74, v73, v71
	v_fma_f32 v75, -v69, v74, v73
	v_fmac_f32_e32 v74, v75, v71
	v_fma_f32 v69, -v69, v74, v73
	v_div_fmas_f32 v69, v69, v71, v74
	v_div_fixup_f32 v110, v69, v68, v110
	ds_write_b32 v33, v110 offset:12288
	s_waitcnt vmcnt(10)
	v_mul_f32_e32 v68, 0xbfb8aa3b, v111
	v_rndne_f32_e32 v69, v68
	v_fma_f32 v72, v111, s6, -v68
	v_sub_f32_e32 v68, v68, v69
	v_fmac_f32_e32 v72, 0xb2a5705f, v111
	v_add_f32_e32 v68, v68, v72
	v_cvt_i32_f32_e32 v69, v69
	v_exp_f32_e32 v68, v68
	v_cmp_nlt_f32_e64 s[22:23], s7, v111
	s_nop 1
	v_ldexp_f32 v68, v68, v69
	v_cndmask_b32_e64 v68, 0, v68, s[22:23]
	v_cmp_ngt_f32_e64 s[22:23], s20, v111
	s_nop 1
	v_cndmask_b32_e64 v68, v97, v68, s[22:23]
	v_add_f32_e32 v68, 1.0, v68
	v_div_scale_f32 v69, s[22:23], v68, v68, v111
	v_rcp_f32_e32 v71, v69
	v_div_scale_f32 v73, vcc, v111, v68, v111
	v_fma_f32 v74, -v69, v71, 1.0
	v_fmac_f32_e32 v71, v74, v71
	v_mul_f32_e32 v74, v73, v71
	v_fma_f32 v75, -v69, v74, v73
	v_fmac_f32_e32 v74, v75, v71
	v_fma_f32 v69, -v69, v74, v73
	v_div_fmas_f32 v69, v69, v71, v74
	v_div_fixup_f32 v111, v69, v68, v111
	ds_write_b32 v33, v111 offset:14336
	s_waitcnt vmcnt(9)
	v_mul_f32_e32 v68, 0xbfb8aa3b, v112
	v_rndne_f32_e32 v69, v68
	v_fma_f32 v72, v112, s6, -v68
	v_sub_f32_e32 v68, v68, v69
	v_fmac_f32_e32 v72, 0xb2a5705f, v112
	v_add_f32_e32 v68, v68, v72
	v_cvt_i32_f32_e32 v69, v69
	v_exp_f32_e32 v68, v68
	v_cmp_nlt_f32_e64 s[22:23], s7, v112
	s_nop 1
	v_ldexp_f32 v68, v68, v69
	v_cndmask_b32_e64 v68, 0, v68, s[22:23]
	v_cmp_ngt_f32_e64 s[22:23], s20, v112
	s_nop 1
	v_cndmask_b32_e64 v68, v97, v68, s[22:23]
	v_add_f32_e32 v68, 1.0, v68
	v_div_scale_f32 v69, s[22:23], v68, v68, v112
	v_rcp_f32_e32 v71, v69
	v_div_scale_f32 v73, vcc, v112, v68, v112
	v_fma_f32 v74, -v69, v71, 1.0
	v_fmac_f32_e32 v71, v74, v71
	v_mul_f32_e32 v74, v73, v71
	v_fma_f32 v75, -v69, v74, v73
	v_fmac_f32_e32 v74, v75, v71
	v_fma_f32 v69, -v69, v74, v73
	v_div_fmas_f32 v69, v69, v71, v74
	v_div_fixup_f32 v112, v69, v68, v112
	ds_write_b32 v33, v112 offset:16384
	s_waitcnt vmcnt(8)
	v_mul_f32_e32 v68, 0xbfb8aa3b, v113
	v_rndne_f32_e32 v69, v68
	v_fma_f32 v72, v113, s6, -v68
	v_sub_f32_e32 v68, v68, v69
	v_fmac_f32_e32 v72, 0xb2a5705f, v113
	v_add_f32_e32 v68, v68, v72
	v_cvt_i32_f32_e32 v69, v69
	v_exp_f32_e32 v68, v68
	v_cmp_nlt_f32_e64 s[22:23], s7, v113
	s_nop 1
	v_ldexp_f32 v68, v68, v69
	v_cndmask_b32_e64 v68, 0, v68, s[22:23]
	v_cmp_ngt_f32_e64 s[22:23], s20, v113
	s_nop 1
	v_cndmask_b32_e64 v68, v97, v68, s[22:23]
	v_add_f32_e32 v68, 1.0, v68
	v_div_scale_f32 v69, s[22:23], v68, v68, v113
	v_rcp_f32_e32 v71, v69
	v_div_scale_f32 v73, vcc, v113, v68, v113
	v_fma_f32 v74, -v69, v71, 1.0
	v_fmac_f32_e32 v71, v74, v71
	v_mul_f32_e32 v74, v73, v71
	v_fma_f32 v75, -v69, v74, v73
	v_fmac_f32_e32 v74, v75, v71
	v_fma_f32 v69, -v69, v74, v73
	v_div_fmas_f32 v69, v69, v71, v74
	v_div_fixup_f32 v113, v69, v68, v113
	ds_write_b32 v33, v113 offset:18432
	s_waitcnt vmcnt(7)
	v_mul_f32_e32 v68, 0xbfb8aa3b, v114
	v_rndne_f32_e32 v69, v68
	v_fma_f32 v72, v114, s6, -v68
	v_sub_f32_e32 v68, v68, v69
	v_fmac_f32_e32 v72, 0xb2a5705f, v114
	v_add_f32_e32 v68, v68, v72
	v_cvt_i32_f32_e32 v69, v69
	v_exp_f32_e32 v68, v68
	v_cmp_nlt_f32_e64 s[22:23], s7, v114
	s_nop 1
	v_ldexp_f32 v68, v68, v69
	v_cndmask_b32_e64 v68, 0, v68, s[22:23]
	v_cmp_ngt_f32_e64 s[22:23], s20, v114
	s_nop 1
	v_cndmask_b32_e64 v68, v97, v68, s[22:23]
	v_add_f32_e32 v68, 1.0, v68
	v_div_scale_f32 v69, s[22:23], v68, v68, v114
	v_rcp_f32_e32 v71, v69
	v_div_scale_f32 v73, vcc, v114, v68, v114
	v_fma_f32 v74, -v69, v71, 1.0
	v_fmac_f32_e32 v71, v74, v71
	v_mul_f32_e32 v74, v73, v71
	v_fma_f32 v75, -v69, v74, v73
	v_fmac_f32_e32 v74, v75, v71
	v_fma_f32 v69, -v69, v74, v73
	v_div_fmas_f32 v69, v69, v71, v74
	v_div_fixup_f32 v114, v69, v68, v114
	ds_write_b32 v33, v114 offset:20480
	s_waitcnt vmcnt(6)
	v_mul_f32_e32 v68, 0xbfb8aa3b, v115
	v_rndne_f32_e32 v69, v68
	v_fma_f32 v72, v115, s6, -v68
	v_sub_f32_e32 v68, v68, v69
	v_fmac_f32_e32 v72, 0xb2a5705f, v115
	v_add_f32_e32 v68, v68, v72
	v_cvt_i32_f32_e32 v69, v69
	v_exp_f32_e32 v68, v68
	v_cmp_nlt_f32_e64 s[22:23], s7, v115
	s_nop 1
	v_ldexp_f32 v68, v68, v69
	v_cndmask_b32_e64 v68, 0, v68, s[22:23]
	v_cmp_ngt_f32_e64 s[22:23], s20, v115
	s_nop 1
	v_cndmask_b32_e64 v68, v97, v68, s[22:23]
	v_add_f32_e32 v68, 1.0, v68
	v_div_scale_f32 v69, s[22:23], v68, v68, v115
	v_rcp_f32_e32 v71, v69
	v_div_scale_f32 v73, vcc, v115, v68, v115
	v_fma_f32 v74, -v69, v71, 1.0
	v_fmac_f32_e32 v71, v74, v71
	v_mul_f32_e32 v74, v73, v71
	v_fma_f32 v75, -v69, v74, v73
	v_fmac_f32_e32 v74, v75, v71
	v_fma_f32 v69, -v69, v74, v73
	v_div_fmas_f32 v69, v69, v71, v74
	v_div_fixup_f32 v115, v69, v68, v115
	ds_write_b32 v33, v115 offset:22528
	s_waitcnt vmcnt(5)
	v_mul_f32_e32 v68, 0xbfb8aa3b, v116
	v_rndne_f32_e32 v69, v68
	v_fma_f32 v72, v116, s6, -v68
	v_sub_f32_e32 v68, v68, v69
	v_fmac_f32_e32 v72, 0xb2a5705f, v116
	v_add_f32_e32 v68, v68, v72
	v_cvt_i32_f32_e32 v69, v69
	v_exp_f32_e32 v68, v68
	v_cmp_nlt_f32_e64 s[22:23], s7, v116
	s_nop 1
	v_ldexp_f32 v68, v68, v69
	v_cndmask_b32_e64 v68, 0, v68, s[22:23]
	v_cmp_ngt_f32_e64 s[22:23], s20, v116
	s_nop 1
	v_cndmask_b32_e64 v68, v97, v68, s[22:23]
	v_add_f32_e32 v68, 1.0, v68
	v_div_scale_f32 v69, s[22:23], v68, v68, v116
	v_rcp_f32_e32 v71, v69
	v_div_scale_f32 v73, vcc, v116, v68, v116
	v_fma_f32 v74, -v69, v71, 1.0
	v_fmac_f32_e32 v71, v74, v71
	v_mul_f32_e32 v74, v73, v71
	v_fma_f32 v75, -v69, v74, v73
	v_fmac_f32_e32 v74, v75, v71
	v_fma_f32 v69, -v69, v74, v73
	v_div_fmas_f32 v69, v69, v71, v74
	v_div_fixup_f32 v116, v69, v68, v116
	ds_write_b32 v33, v116 offset:24576
	s_waitcnt vmcnt(4)
	v_mul_f32_e32 v68, 0xbfb8aa3b, v117
	v_rndne_f32_e32 v69, v68
	v_fma_f32 v72, v117, s6, -v68
	v_sub_f32_e32 v68, v68, v69
	v_fmac_f32_e32 v72, 0xb2a5705f, v117
	v_add_f32_e32 v68, v68, v72
	v_cvt_i32_f32_e32 v69, v69
	v_exp_f32_e32 v68, v68
	v_cmp_nlt_f32_e64 s[22:23], s7, v117
	s_nop 1
	v_ldexp_f32 v68, v68, v69
	v_cndmask_b32_e64 v68, 0, v68, s[22:23]
	v_cmp_ngt_f32_e64 s[22:23], s20, v117
	s_nop 1
	v_cndmask_b32_e64 v68, v97, v68, s[22:23]
	v_add_f32_e32 v68, 1.0, v68
	v_div_scale_f32 v69, s[22:23], v68, v68, v117
	v_rcp_f32_e32 v71, v69
	v_div_scale_f32 v73, vcc, v117, v68, v117
	v_fma_f32 v74, -v69, v71, 1.0
	v_fmac_f32_e32 v71, v74, v71
	v_mul_f32_e32 v74, v73, v71
	v_fma_f32 v75, -v69, v74, v73
	v_fmac_f32_e32 v74, v75, v71
	v_fma_f32 v69, -v69, v74, v73
	v_div_fmas_f32 v69, v69, v71, v74
	v_div_fixup_f32 v117, v69, v68, v117
	ds_write_b32 v33, v117 offset:26624
	s_waitcnt vmcnt(3)
	v_mul_f32_e32 v68, 0xbfb8aa3b, v118
	v_rndne_f32_e32 v69, v68
	v_fma_f32 v72, v118, s6, -v68
	v_sub_f32_e32 v68, v68, v69
	v_fmac_f32_e32 v72, 0xb2a5705f, v118
	v_add_f32_e32 v68, v68, v72
	v_cvt_i32_f32_e32 v69, v69
	v_exp_f32_e32 v68, v68
	v_cmp_nlt_f32_e64 s[22:23], s7, v118
	s_nop 1
	v_ldexp_f32 v68, v68, v69
	v_cndmask_b32_e64 v68, 0, v68, s[22:23]
	v_cmp_ngt_f32_e64 s[22:23], s20, v118
	s_nop 1
	v_cndmask_b32_e64 v68, v97, v68, s[22:23]
	v_add_f32_e32 v68, 1.0, v68
	v_div_scale_f32 v69, s[22:23], v68, v68, v118
	v_rcp_f32_e32 v71, v69
	v_div_scale_f32 v73, vcc, v118, v68, v118
	v_fma_f32 v74, -v69, v71, 1.0
	v_fmac_f32_e32 v71, v74, v71
	v_mul_f32_e32 v74, v73, v71
	v_fma_f32 v75, -v69, v74, v73
	v_fmac_f32_e32 v74, v75, v71
	v_fma_f32 v69, -v69, v74, v73
	v_div_fmas_f32 v69, v69, v71, v74
	v_div_fixup_f32 v118, v69, v68, v118
	ds_write_b32 v33, v118 offset:28672
	s_waitcnt vmcnt(2)
	v_mul_f32_e32 v68, 0xbfb8aa3b, v119
	v_rndne_f32_e32 v69, v68
	v_fma_f32 v72, v119, s6, -v68
	v_sub_f32_e32 v68, v68, v69
	v_fmac_f32_e32 v72, 0xb2a5705f, v119
	v_add_f32_e32 v68, v68, v72
	v_cvt_i32_f32_e32 v69, v69
	v_exp_f32_e32 v68, v68
	v_cmp_nlt_f32_e64 s[22:23], s7, v119
	s_nop 1
	v_ldexp_f32 v68, v68, v69
	v_cndmask_b32_e64 v68, 0, v68, s[22:23]
	v_cmp_ngt_f32_e64 s[22:23], s20, v119
	s_nop 1
	v_cndmask_b32_e64 v68, v97, v68, s[22:23]
	v_add_f32_e32 v68, 1.0, v68
	v_div_scale_f32 v69, s[22:23], v68, v68, v119
	v_rcp_f32_e32 v71, v69
	v_div_scale_f32 v73, vcc, v119, v68, v119
	v_fma_f32 v74, -v69, v71, 1.0
	v_fmac_f32_e32 v71, v74, v71
	v_mul_f32_e32 v74, v73, v71
	v_fma_f32 v75, -v69, v74, v73
	v_fmac_f32_e32 v74, v75, v71
	v_fma_f32 v69, -v69, v74, v73
	v_div_fmas_f32 v69, v69, v71, v74
	v_div_fixup_f32 v119, v69, v68, v119
	ds_write_b32 v33, v119 offset:30720
	s_waitcnt vmcnt(1)
	v_mul_f32_e32 v68, 0xbfb8aa3b, v120
	v_rndne_f32_e32 v69, v68
	v_fma_f32 v72, v120, s6, -v68
	v_sub_f32_e32 v68, v68, v69
	v_fmac_f32_e32 v72, 0xb2a5705f, v120
	v_add_f32_e32 v68, v68, v72
	v_cvt_i32_f32_e32 v69, v69
	v_exp_f32_e32 v68, v68
	v_cmp_nlt_f32_e64 s[22:23], s7, v120
	s_nop 1
	v_ldexp_f32 v68, v68, v69
	v_cndmask_b32_e64 v68, 0, v68, s[22:23]
	v_cmp_ngt_f32_e64 s[22:23], s20, v120
	s_nop 1
	v_cndmask_b32_e64 v68, v97, v68, s[22:23]
	v_add_f32_e32 v68, 1.0, v68
	v_div_scale_f32 v69, s[22:23], v68, v68, v120
	v_rcp_f32_e32 v71, v69
	v_div_scale_f32 v73, vcc, v120, v68, v120
	v_fma_f32 v74, -v69, v71, 1.0
	v_fmac_f32_e32 v71, v74, v71
	v_mul_f32_e32 v74, v73, v71
	v_fma_f32 v75, -v69, v74, v73
	v_fmac_f32_e32 v74, v75, v71
	v_fma_f32 v69, -v69, v74, v73
	v_div_fmas_f32 v69, v69, v71, v74
	v_div_fixup_f32 v120, v69, v68, v120
	ds_write_b32 v33, v120 offset:32768
	s_waitcnt vmcnt(0)
	v_mul_f32_e32 v68, 0xbfb8aa3b, v121
	v_rndne_f32_e32 v69, v68
	v_fma_f32 v72, v121, s6, -v68
	v_sub_f32_e32 v68, v68, v69
	v_fmac_f32_e32 v72, 0xb2a5705f, v121
	v_add_f32_e32 v68, v68, v72
	v_cvt_i32_f32_e32 v69, v69
	v_exp_f32_e32 v68, v68
	v_cmp_nlt_f32_e64 s[22:23], s7, v121
	s_nop 1
	v_ldexp_f32 v68, v68, v69
	v_cndmask_b32_e64 v68, 0, v68, s[22:23]
	v_cmp_ngt_f32_e64 s[22:23], s20, v121
	s_nop 1
	v_cndmask_b32_e64 v68, v97, v68, s[22:23]
	v_add_f32_e32 v68, 1.0, v68
	v_div_scale_f32 v69, s[22:23], v68, v68, v121
	v_rcp_f32_e32 v71, v69
	v_div_scale_f32 v73, vcc, v121, v68, v121
	v_fma_f32 v74, -v69, v71, 1.0
	v_fmac_f32_e32 v71, v74, v71
	v_mul_f32_e32 v74, v73, v71
	v_fma_f32 v75, -v69, v74, v73
	v_fmac_f32_e32 v74, v75, v71
	v_fma_f32 v69, -v69, v74, v73
	v_div_fmas_f32 v69, v69, v71, v74
	v_div_fixup_f32 v121, v69, v68, v121
	ds_write_b32 v33, v121 offset:34816
